# v63 plus s_sleep 6 per item in the layer-0 projector loop (less burst traffic while the first recurrent steps run)
# baseline (speedup 1.0000x reference)
.LBB0_13:
	v_add_u32_e32 v70, 2, v70
	v_cndmask_b32_e64 v66, v71, v70, s[6:7]
	v_lshl_or_b32 v66, v66, 13, v75
	v_lshl_add_u64 v[80:81], v[68:69], 0, v[66:67]
	global_load_dwordx4 v[76:79], v[80:81], off
	global_load_dwordx4 v[86:89], v[80:81], off offset:64
	global_load_dwordx4 v[94:97], v[80:81], off offset:128
	global_load_dwordx4 v[98:101], v[80:81], off offset:192
	global_load_dwordx4 v[102:105], v[80:81], off offset:256
	global_load_dwordx4 v[106:109], v[80:81], off offset:320
	global_load_dwordx4 v[110:113], v[80:81], off offset:384
	global_load_dwordx4 v[114:117], v[80:81], off offset:448
	v_cmp_lt_u32_e32 vcc, 27, v70
	v_add_u32_e32 v71, -2, v71
	s_or_b64 s[28:29], vcc, s[28:29]
	s_waitcnt vmcnt(7)
	v_mfma_f32_16x16x32_f16 a[8:11], v[2:5], v[76:79], a[0:3]
	v_mfma_f32_16x16x32_f16 a[12:15], v[30:33], v[76:79], a[4:7]
	s_waitcnt vmcnt(6)
	v_mfma_f32_16x16x32_f16 a[8:11], v[6:9], v[86:89], a[8:11]
	v_mfma_f32_16x16x32_f16 a[12:15], v[34:37], v[86:89], a[12:15]
	s_waitcnt vmcnt(5)
	v_mfma_f32_16x16x32_f16 a[8:11], v[10:13], v[94:97], a[8:11]
	v_mfma_f32_16x16x32_f16 a[12:15], v[38:41], v[94:97], a[12:15]
	s_waitcnt vmcnt(4)
	v_mfma_f32_16x16x32_f16 a[8:11], v[14:17], v[98:101], a[8:11]
	v_mfma_f32_16x16x32_f16 a[12:15], v[42:45], v[98:101], a[12:15]
	s_waitcnt vmcnt(3)
	v_mfma_f32_16x16x32_f16 a[8:11], v[26:29], v[102:105], a[8:11]
	v_mfma_f32_16x16x32_f16 a[12:15], v[50:53], v[102:105], a[12:15]
	s_waitcnt vmcnt(2)
	v_mfma_f32_16x16x32_f16 a[8:11], v[18:21], v[106:109], a[8:11]
	v_mfma_f32_16x16x32_f16 a[12:15], v[54:57], v[106:109], a[12:15]
	s_waitcnt vmcnt(1)
	v_mfma_f32_16x16x32_f16 a[8:11], v[22:25], v[110:113], a[8:11]
	v_mfma_f32_16x16x32_f16 a[12:15], v[58:61], v[110:113], a[12:15]
	s_waitcnt vmcnt(0)
	v_mfma_f32_16x16x32_f16 a[8:11], v[46:49], v[114:117], a[8:11]
	v_mfma_f32_16x16x32_f16 a[12:15], v[62:65], v[114:117], a[12:15]
	s_nop 6
	ds_write_b128 v73, a[8:11]
	ds_write_b128 v73, a[12:15] offset:1024
	v_add_u32_e32 v73, 0x1000, v73
	ds_write_b32 v72, v74
	v_add_u32_e32 v72, 8, v72
	s_sleep 6
	s_andn2_b64 exec, exec, s[28:29]
	s_cbranch_execnz .LBB0_13
	s_or_b64 exec, exec, s[28:29]
	s_lshl_b64 s[4:5], s[4:5], 15
	s_add_u32 s4, s40, s4
	s_addc_u32 s5, s41, s5
	v_lshlrev_b32_e32 v194, 4, v130
	v_mov_b32_e32 v195, 0
	v_lshl_add_u64 v[110:111], s[4:5], 0, v[194:195]
	global_load_dwordx4 v[2:5], v194, s[4:5]
	global_load_dwordx4 v[6:9], v194, s[4:5] offset:1024
	global_load_dwordx4 v[10:13], v194, s[4:5] offset:2048
	global_load_dwordx4 v[14:17], v194, s[4:5] offset:3072
	s_movk_i32 s4, 0x1000
	v_add_co_u32_e32 v86, vcc, s4, v110
	s_movk_i32 s4, 0x2000
	s_nop 0
	v_addc_co_u32_e32 v87, vcc, 0, v111, vcc
	v_add_co_u32_e32 v88, vcc, s4, v110
	s_movk_i32 s4, 0x3000
	s_nop 0
	v_addc_co_u32_e32 v89, vcc, 0, v111, vcc
	v_add_co_u32_e32 v90, vcc, s4, v110
	s_movk_i32 s4, 0x4000
	s_nop 0
	v_addc_co_u32_e32 v91, vcc, 0, v111, vcc
	v_add_co_u32_e32 v92, vcc, s4, v110
	s_movk_i32 s4, 0x5000
	s_nop 0
	v_addc_co_u32_e32 v93, vcc, 0, v111, vcc
	s_lshl_b32 s28, s30, 2
	v_add_co_u32_e32 v112, vcc, s4, v110
	s_add_u32 s4, s48, s28
	s_addc_u32 s5, s49, 0
	global_load_dwordx4 v[18:21], v[86:87], off offset:1024
	global_load_dwordx4 v[22:25], v[86:87], off offset:2048
	global_load_dwordx4 v[26:29], v[88:89], off offset:-4096
	global_load_dwordx4 v[30:33], v[88:89], off
	global_load_dwordx4 v[34:37], v[88:89], off offset:1024
	global_load_dwordx4 v[38:41], v[88:89], off offset:2048
	global_load_dwordx4 v[42:45], v[88:89], off offset:3072
	global_load_dwordx4 v[46:49], v[92:93], off offset:-4096
	global_load_dwordx4 v[50:53], v[86:87], off offset:3072
	global_load_dwordx4 v[54:57], v[90:91], off offset:1024
	global_load_dwordx4 v[58:61], v[90:91], off offset:2048
	global_load_dwordx4 v[62:65], v[90:91], off offset:3072
	global_load_dwordx4 v[66:69], v[92:93], off
	global_load_dwordx4 v[70:73], v[92:93], off offset:1024
	global_load_dwordx4 v[74:77], v[92:93], off offset:2048
	global_load_dwordx4 v[78:81], v[92:93], off offset:3072
	v_lshl_add_u64 v[86:87], s[4:5], 0, v[82:83]
	s_add_u32 s4, s50, s28
	s_addc_u32 s5, s51, 0
	v_addc_co_u32_e32 v113, vcc, 0, v111, vcc
	v_lshl_add_u64 v[82:83], s[4:5], 0, v[82:83]
	s_movk_i32 s4, 0x6000
	v_lshlrev_b32_e32 v194, 2, v84
	v_add_co_u32_e32 v106, vcc, s4, v110
	v_lshl_add_u64 v[84:85], v[86:87], 0, v[194:195]
	v_lshl_add_u64 v[82:83], v[82:83], 0, v[194:195]
	v_addc_co_u32_e32 v107, vcc, 0, v111, vcc
	s_movk_i32 s4, 0x7000
	global_load_dwordx4 v[138:141], v[84:85], off
	global_load_dwordx4 v[142:145], v[82:83], off
	global_load_dwordx4 v[146:149], v[84:85], off offset:2048
	global_load_dwordx4 v[150:153], v[82:83], off offset:2048
	s_nop 0
	global_load_dwordx4 v[82:85], v[112:113], off offset:1024
	global_load_dwordx4 v[86:89], v[112:113], off offset:2048
	global_load_dwordx4 v[90:93], v[106:107], off offset:-4096
	global_load_dwordx4 v[94:97], v[106:107], off
	global_load_dwordx4 v[98:101], v[106:107], off offset:1024
	global_load_dwordx4 v[102:105], v[106:107], off offset:2048
	s_nop 0
	global_load_dwordx4 v[106:109], v[106:107], off offset:3072
	v_add_co_u32_e32 v126, vcc, s4, v110
	s_mov_b32 s4, 0xbfb8aa3b
	s_nop 0
	v_addc_co_u32_e32 v127, vcc, 0, v111, vcc
	global_load_dwordx4 v[110:113], v[112:113], off offset:3072
	s_nop 0
	global_load_dwordx4 v[114:117], v[126:127], off
	global_load_dwordx4 v[118:121], v[126:127], off offset:1024
	global_load_dwordx4 v[122:125], v[126:127], off offset:2048
	s_nop 0
	global_load_dwordx4 v[126:129], v[126:127], off offset:3072
	v_add_u32_e32 v204, -1, v1
	v_lshl_add_u32 v1, v130, 4, 0
	v_and_b32_e32 v130, 0x78, v131
	v_lshl_or_b32 v205, v136, 7, v130
	v_or_b32_e32 v206, 0x1e000, v205
	s_mov_b64 s[28:29], 0
	s_mov_b64 s[30:31], 0x1000
	s_mov_b32 s40, 0xfffeffff
	v_mov_b32_e32 v207, 2
	s_waitcnt vmcnt(14)
	v_pk_add_f32 v[138:139], v[138:139], v[142:143]
	v_pk_add_f32 v[140:141], v[140:141], v[144:145]
	s_waitcnt vmcnt(12)
	v_pk_add_f32 v[142:143], v[146:147], v[150:151]
	v_pk_mul_f32 v[140:141], v[140:141], s[4:5] op_sel_hi:[1,0]
	v_pk_mul_f32 v[138:139], v[138:139], s[4:5] op_sel_hi:[1,0]
	v_pk_add_f32 v[144:145], v[148:149], v[152:153]
	v_pk_mul_f32 v[132:133], v[132:133], v[142:143]
	s_and_b64 s[4:5], s[6:7], exec
	v_pk_mul_f32 v[134:135], v[134:135], v[144:145]
	s_cselect_b32 s38, -8, -1
	s_cmp_eq_u32 s3, 1
	v_accvgpr_write_b32 a0, v138
	v_accvgpr_write_b32 a4, v132
	s_cselect_b32 s39, -8, -1
	v_cmp_eq_u32_e64 s[4:5], 0, v204
	v_accvgpr_write_b32 a1, v139
	v_accvgpr_write_b32 a2, v140
	v_accvgpr_write_b32 a3, v141
	v_accvgpr_write_b32 a5, v133
	v_accvgpr_write_b32 a6, v134
	v_accvgpr_write_b32 a7, v135
	s_branch .LBB0_16
